# v15 + the 7 non-leader waves of each workgroup copy one expert-weight tile while the leader runs the grid-barrier protocol (12 of the 18 barriers; router phases keep the rest)
# baseline (speedup 1.0000x reference)
; #define LAS __attribute__((address_space(3)))
; template <class T> __device__ __forceinline__ T* wsp(const Frame& F, size_t off) { return (T*)(F.ws + off); }
; __device__ __forceinline__ void xcd_barrier(const XcdBarrier& b) {
;     asm volatile("s_waitcnt vmcnt(0)" ::: "memory");
;     __syncthreads();
;     if (threadIdx.x == 0) {
;         unsigned* bar = b.bar;
;         __builtin_amdgcn_s_waitcnt(0);
;     LAS float* scr = (LAS float*)(F.lds + RING_OFF + F.wave * 16384);
;     const int gw = (ncu ? (int)blockIdx.x - cu0 : F.vcu) * NWAVES + F.wave, NGW = (ncu ? ncu : F.G) * NWAVES;
;     bf16* UP = wsp<bf16>(F, WS_WEUP); bf16* DN = wsp<bf16>(F, WS_WEDN);
;     for (int it = it0 + gw; it < it1; it += NGW) {
;         const int e = it / 384, r = it % 384; const size_t eo = (size_t)(layer * 64 + e) * 1024 * 256;
;         if (r < 128) p0_transpose_item(inp(F, I_WGATE) + eo, 1024, 256, UP + (size_t)e * 512 * 1024, 3, scr, r, F.lane);
;         else if (r < 256) p0_transpose_item(inp(F, I_WUP) + eo, 1024, 256, UP + (size_t)e * 512 * 1024, 4, scr, r - 128, F.lane);
;         else p0_transpose_item(inp(F, I_WDOWN) + eo, 256, 1024, DN + (size_t)e * 1024 * 256, 5, scr, r - 256, F.lane, 16.f);
.LBB0_185:
	s_or_b64 exec, exec, s[12:13]
	s_waitcnt vmcnt(0)
	s_branch .LBB0_186
.Lb0_entry:
	s_mov_b64 exec, s[2:3]
	s_cmpk_lg_i32 s67, 0x100
	s_cbranch_scc1 .Lb0_out
	v_writelane_b32 v250, s2, 0
	v_writelane_b32 v250, s3, 1
	v_writelane_b32 v250, s4, 2
	v_writelane_b32 v250, s5, 3
	v_writelane_b32 v250, s9, 4
	v_writelane_b32 v250, s10, 5
	v_writelane_b32 v250, s11, 6
	v_writelane_b32 v250, s12, 7
	v_writelane_b32 v250, s13, 8
	v_writelane_b32 v250, s14, 9
	v_writelane_b32 v250, s15, 10
	v_writelane_b32 v250, s16, 11
	v_writelane_b32 v250, s17, 12
	v_writelane_b32 v250, s18, 13
	v_writelane_b32 v250, s19, 14
	v_writelane_b32 v250, s20, 15
	v_writelane_b32 v250, s21, 16
	v_writelane_b32 v250, s22, 17
	v_writelane_b32 v250, s23, 18
	v_writelane_b32 v250, s30, 19
	v_writelane_b32 v250, s31, 20
	v_writelane_b32 v250, s40, 21
	v_writelane_b32 v250, s41, 22
	v_writelane_b32 v250, s42, 23
	v_writelane_b32 v250, s43, 24
	v_writelane_b32 v250, s44, 25
	v_writelane_b32 v250, s45, 26
	v_writelane_b32 v250, s46, 27
	v_writelane_b32 v250, s47, 28
	v_writelane_b32 v250, s48, 29
	v_writelane_b32 v250, s49, 30
	v_writelane_b32 v250, s50, 31
	v_writelane_b32 v250, s51, 32
	v_writelane_b32 v250, s52, 33
	v_writelane_b32 v250, s53, 34
	v_writelane_b32 v250, s54, 35
	v_writelane_b32 v250, s56, 36
	v_writelane_b32 v250, s57, 37
	v_writelane_b32 v250, vcc_lo, 38
	v_writelane_b32 v250, vcc_hi, 39
	v_mov_b32_e32 v2, v0
	s_mul_i32 s4, s71, 7
	s_movk_i32 s2, 0x6000
	v_readfirstlane_b32 s5, v2
	s_movk_i32 s3, 0x2000
	s_ashr_i32 s5, s5, 6
	s_add_i32 s5, s5, s4
	s_add_i32 s5, s5, 0x23ff
	s_cmpk_gt_i32 s5, 0x2aff
	s_cbranch_scc1 .Lb0_end
	s_add_u32 s9, s26, 0x4800000
	s_addc_u32 s18, s27, 0
	s_add_u32 s19, s26, 0x2800000
	v_and_b32_e32 v1, 56, v2
	v_lshlrev_b32_e32 v2, 2, v2
	s_addc_u32 s20, s27, 0
	v_and_b32_e32 v10, 28, v2
	s_lshl_b32 s21, s5, 6
	s_lshl_b32 s22, s2, 6
	s_lshl_b32 s23, s5, 5
	s_lshl_b32 s40, s2, 5
	s_lshl_b32 s41, s5, 3
	s_lshl_b32 s42, s2, 3
	s_lshl_b32 s43, s5, 1
	s_lshl_b32 s44, s2, 1
	s_add_i32 s45, 0, 0x202a8
	s_waitcnt lgkmcnt(1)
	v_mov_b32_e32 v7, 0
	s_movk_i32 s46, 0x1000
	s_movk_i32 s47, 0x4000
	s_movk_i32 s48, 0x6000
	s_movk_i32 s49, 0x7000
	s_mov_b32 s4, 0x41800000
	s_movk_i32 s50, 0x7fff
	s_mov_b32 s51, 0xffff0000
	s_mov_b64 s[10:11], 0x600
	s_add_i32 s52, 0, 0x202a0
	s_add_i32 s53, 0, 0x20298
	v_mov_b32_e32 v11, 1
	v_mov_b32_e32 v12, 0x400
	v_mov_b32_e32 v13, 0x7c
	s_branch .Lb0_07

;     __device__ __forceinline__ void st(const void* p, const u32x4& v) const { __builtin_amdgcn_raw_buffer_store_b128(v, r, (unsigned)((const unsigned char*)p - b), 0, EPI_SC1); }
; __device__ __forceinline__ unsigned xb_ld(unsigned* p)              { return __hip_atomic_load(p, __ATOMIC_RELAXED, __HIP_MEMORY_SCOPE_AGENT); }
; __device__ __forceinline__ unsigned xb_add(unsigned* p, unsigned v) { return __hip_atomic_fetch_add(p, v, __ATOMIC_RELAXED, __HIP_MEMORY_SCOPE_AGENT); }
; #define XB_SPIN(cond, bar) do { unsigned _sp = 0; while (cond) { __builtin_amdgcn_s_sleep(1); \
;     if ((++_sp & 255u) == 0u) { if (xb_ld(&(bar)[XB_TMO])) break; if (_sp > XB_SPIN_CAP) { atomicAdd(&(bar)[XB_TMO], 1u); break; } } } } while (0)
; __device__ __forceinline__ void xcd_barrier(const XcdBarrier& b) {
;     asm volatile("s_waitcnt vmcnt(0)" ::: "memory");
;     __syncthreads();
;     if (threadIdx.x == 0) {
;         unsigned* bar = b.bar;
;         __builtin_amdgcn_s_waitcnt(0);
;         unsigned nloc = b.st[0], nx = b.st[1];
;         if (nloc == 0u) { xcd_barrier_complete(bar, b.x, nloc, nx); b.st[0] = nloc; b.st[1] = nx; }
;         const unsigned old = xb_add(&bar[XB_XSUB(b.x)], 1u);
;         const unsigned gen = old / nloc;
;         if (old + 1u == (gen + 1u) * nloc) {
;             __builtin_amdgcn_fence(__ATOMIC_RELEASE, "agent");
;             asm volatile("s_waitcnt vmcnt(0)" ::: "memory");
;             const unsigned og = xb_add(&bar[XB_TOP], 1u);
;             const unsigned tg = og / nx;
;             if (og + 1u == (tg + 1u) * nx) xb_add(&bar[XB_TOPGEN], 1u);
;             else XB_SPIN(xb_ld(&bar[XB_TOPGEN]) == tg, bar);
;             __builtin_amdgcn_fence(__ATOMIC_ACQUIRE, "agent");
;             xb_add(&bar[XB_XGEN(b.x)], 1u);
;             asm volatile("s_waitcnt vmcnt(0)" ::: "memory");
;         } else {
;             XB_SPIN(xb_ld(&bar[XB_XGEN(b.x)]) == gen, bar);
;             __builtin_amdgcn_fence(__ATOMIC_ACQUIRE, "agent");
;             asm volatile("s_waitcnt vmcnt(0)" ::: "memory");
;         }
;     }
;     __syncthreads();
; }
.Lb0_end:
	v_readlane_b32 s2, v250, 0
	v_readlane_b32 s3, v250, 1
	v_readlane_b32 s4, v250, 2
	v_readlane_b32 s5, v250, 3
	v_readlane_b32 s9, v250, 4
	v_readlane_b32 s10, v250, 5
	v_readlane_b32 s11, v250, 6
	v_readlane_b32 s12, v250, 7
	v_readlane_b32 s13, v250, 8
	v_readlane_b32 s14, v250, 9
	v_readlane_b32 s15, v250, 10
	v_readlane_b32 s16, v250, 11
	v_readlane_b32 s17, v250, 12
	v_readlane_b32 s18, v250, 13
	v_readlane_b32 s19, v250, 14
	v_readlane_b32 s20, v250, 15
	v_readlane_b32 s21, v250, 16
	v_readlane_b32 s22, v250, 17
	v_readlane_b32 s23, v250, 18
	v_readlane_b32 s30, v250, 19
	v_readlane_b32 s31, v250, 20
	v_readlane_b32 s40, v250, 21
	v_readlane_b32 s41, v250, 22
	v_readlane_b32 s42, v250, 23
	v_readlane_b32 s43, v250, 24
	v_readlane_b32 s44, v250, 25
	v_readlane_b32 s45, v250, 26
	v_readlane_b32 s46, v250, 27
	v_readlane_b32 s47, v250, 28
	v_readlane_b32 s48, v250, 29
	v_readlane_b32 s49, v250, 30
	v_readlane_b32 s50, v250, 31
	v_readlane_b32 s51, v250, 32
	v_readlane_b32 s52, v250, 33
	v_readlane_b32 s53, v250, 34
	v_readlane_b32 s54, v250, 35
	v_readlane_b32 s56, v250, 36
	v_readlane_b32 s57, v250, 37
	v_readlane_b32 vcc_lo, v250, 38
	v_readlane_b32 vcc_hi, v250, 39
.Lb0_out:
.LBB0_186:
	s_or_b64 exec, exec, s[2:3]
	s_waitcnt lgkmcnt(0)
	s_barrier

; #define LAS __attribute__((address_space(3)))
; template <class T> __device__ __forceinline__ T* wsp(const Frame& F, size_t off) { return (T*)(F.ws + off); }
; __device__ __forceinline__ void xcd_barrier(const XcdBarrier& b) {
;     asm volatile("s_waitcnt vmcnt(0)" ::: "memory");
;     __syncthreads();
;     if (threadIdx.x == 0) {
;         unsigned* bar = b.bar;
;         __builtin_amdgcn_s_waitcnt(0);
;     LAS float* scr = (LAS float*)(F.lds + RING_OFF + F.wave * 16384);
;     const int gw = (ncu ? (int)blockIdx.x - cu0 : F.vcu) * NWAVES + F.wave, NGW = (ncu ? ncu : F.G) * NWAVES;
;     bf16* UP = wsp<bf16>(F, WS_WEUP); bf16* DN = wsp<bf16>(F, WS_WEDN);
;     for (int it = it0 + gw; it < it1; it += NGW) {
;         const int e = it / 384, r = it % 384; const size_t eo = (size_t)(layer * 64 + e) * 1024 * 256;
;         if (r < 128) p0_transpose_item(inp(F, I_WGATE) + eo, 1024, 256, UP + (size_t)e * 512 * 1024, 3, scr, r, F.lane);
;         else if (r < 256) p0_transpose_item(inp(F, I_WUP) + eo, 1024, 256, UP + (size_t)e * 512 * 1024, 4, scr, r - 128, F.lane);
;         else p0_transpose_item(inp(F, I_WDOWN) + eo, 256, 1024, DN + (size_t)e * 1024 * 256, 5, scr, r - 256, F.lane, 16.f);
.Lb1_entry:
	s_mov_b64 exec, s[0:1]
	s_cmpk_lg_i32 s67, 0x100
	s_cbranch_scc1 .Lb1_out
	v_writelane_b32 v250, s2, 0
	v_writelane_b32 v250, s3, 1
	v_writelane_b32 v250, s4, 2
	v_writelane_b32 v250, s5, 3
	v_writelane_b32 v250, s9, 4
	v_writelane_b32 v250, s10, 5
	v_writelane_b32 v250, s11, 6
	v_writelane_b32 v250, s12, 7
	v_writelane_b32 v250, s13, 8
	v_writelane_b32 v250, s14, 9
	v_writelane_b32 v250, s15, 10
	v_writelane_b32 v250, s16, 11
	v_writelane_b32 v250, s17, 12
	v_writelane_b32 v250, s18, 13
	v_writelane_b32 v250, s19, 14
	v_writelane_b32 v250, s20, 15
	v_writelane_b32 v250, s21, 16
	v_writelane_b32 v250, s22, 17
	v_writelane_b32 v250, s23, 18
	v_writelane_b32 v250, s30, 19
	v_writelane_b32 v250, s31, 20
	v_writelane_b32 v250, s40, 21
	v_writelane_b32 v250, s41, 22
	v_writelane_b32 v250, s42, 23
	v_writelane_b32 v250, s43, 24
	v_writelane_b32 v250, s44, 25
	v_writelane_b32 v250, s45, 26
	v_writelane_b32 v250, s46, 27
	v_writelane_b32 v250, s47, 28
	v_writelane_b32 v250, s48, 29
	v_writelane_b32 v250, s49, 30
	v_writelane_b32 v250, s50, 31
	v_writelane_b32 v250, s51, 32
	v_writelane_b32 v250, s52, 33
	v_writelane_b32 v250, s53, 34
	v_writelane_b32 v250, s54, 35
	v_writelane_b32 v250, s56, 36
	v_writelane_b32 v250, s57, 37
	v_writelane_b32 v250, vcc_lo, 38
	v_writelane_b32 v250, vcc_hi, 39
	v_mov_b32_e32 v2, v0
	s_mul_i32 s4, s71, 7
	s_movk_i32 s2, 0x6000
	v_readfirstlane_b32 s5, v2
	s_movk_i32 s3, 0x2000
	s_ashr_i32 s5, s5, 6
	s_add_i32 s5, s5, s4
	s_add_i32 s5, s5, 0x2aff
	s_cmpk_gt_i32 s5, 0x31ff
	s_cbranch_scc1 .Lb1_end
	s_add_u32 s9, s26, 0x4800000
	s_addc_u32 s18, s27, 0
	s_add_u32 s19, s26, 0x2800000
	v_and_b32_e32 v1, 56, v2
	v_lshlrev_b32_e32 v2, 2, v2
	s_addc_u32 s20, s27, 0
	v_and_b32_e32 v10, 28, v2
	s_lshl_b32 s21, s5, 6
	s_lshl_b32 s22, s2, 6
	s_lshl_b32 s23, s5, 5
	s_lshl_b32 s40, s2, 5
	s_lshl_b32 s41, s5, 3
	s_lshl_b32 s42, s2, 3
	s_lshl_b32 s43, s5, 1
	s_lshl_b32 s44, s2, 1
	s_add_i32 s45, 0, 0x202a8
	s_waitcnt lgkmcnt(1)
	v_mov_b32_e32 v7, 0
	s_movk_i32 s46, 0x1000
	s_movk_i32 s47, 0x4000
	s_movk_i32 s48, 0x6000
	s_movk_i32 s49, 0x7000
	s_mov_b32 s4, 0x41800000
	s_movk_i32 s50, 0x7fff
	s_mov_b32 s51, 0xffff0000
	s_mov_b64 s[10:11], 0x600
	s_add_i32 s52, 0, 0x202a0
	s_add_i32 s53, 0, 0x20298
	v_mov_b32_e32 v11, 1
	v_mov_b32_e32 v12, 0x400
	v_mov_b32_e32 v13, 0x7c
	s_branch .Lb1_07

; __device__ __forceinline__ void xcd_barrier(const XcdBarrier& b) {
;     ...
;     }
;     __syncthreads();
.Lb1_out:
.LBB0_250:
	s_or_b64 exec, exec, s[0:1]
	s_waitcnt lgkmcnt(0)
	s_barrier

; #define LAS __attribute__((address_space(3)))
; template <class T> __device__ __forceinline__ T* wsp(const Frame& F, size_t off) { return (T*)(F.ws + off); }
; __device__ __forceinline__ void xcd_barrier(const XcdBarrier& b) {
;     asm volatile("s_waitcnt vmcnt(0)" ::: "memory");
;     __syncthreads();
;     if (threadIdx.x == 0) {
;         unsigned* bar = b.bar;
;         __builtin_amdgcn_s_waitcnt(0);
;     LAS float* scr = (LAS float*)(F.lds + RING_OFF + F.wave * 16384);
;     const int gw = (ncu ? (int)blockIdx.x - cu0 : F.vcu) * NWAVES + F.wave, NGW = (ncu ? ncu : F.G) * NWAVES;
;     bf16* UP = wsp<bf16>(F, WS_WEUP); bf16* DN = wsp<bf16>(F, WS_WEDN);
;     for (int it = it0 + gw; it < it1; it += NGW) {
;         const int e = it / 384, r = it % 384; const size_t eo = (size_t)(layer * 64 + e) * 1024 * 256;
;         if (r < 128) p0_transpose_item(inp(F, I_WGATE) + eo, 1024, 256, UP + (size_t)e * 512 * 1024, 3, scr, r, F.lane);
;         else if (r < 256) p0_transpose_item(inp(F, I_WUP) + eo, 1024, 256, UP + (size_t)e * 512 * 1024, 4, scr, r - 128, F.lane);
;         else p0_transpose_item(inp(F, I_WDOWN) + eo, 256, 1024, DN + (size_t)e * 1024 * 256, 5, scr, r - 256, F.lane, 16.f);
.Lb2_entry:
	s_mov_b64 exec, s[0:1]
	s_cmpk_lg_i32 s67, 0x100
	s_cbranch_scc1 .Lb2_out
	v_writelane_b32 v250, s2, 0
	v_writelane_b32 v250, s3, 1
	v_writelane_b32 v250, s4, 2
	v_writelane_b32 v250, s5, 3
	v_writelane_b32 v250, s9, 4
	v_writelane_b32 v250, s10, 5
	v_writelane_b32 v250, s11, 6
	v_writelane_b32 v250, s12, 7
	v_writelane_b32 v250, s13, 8
	v_writelane_b32 v250, s14, 9
	v_writelane_b32 v250, s15, 10
	v_writelane_b32 v250, s16, 11
	v_writelane_b32 v250, s17, 12
	v_writelane_b32 v250, s18, 13
	v_writelane_b32 v250, s19, 14
	v_writelane_b32 v250, s20, 15
	v_writelane_b32 v250, s21, 16
	v_writelane_b32 v250, s22, 17
	v_writelane_b32 v250, s23, 18
	v_writelane_b32 v250, s30, 19
	v_writelane_b32 v250, s31, 20
	v_writelane_b32 v250, s40, 21
	v_writelane_b32 v250, s41, 22
	v_writelane_b32 v250, s42, 23
	v_writelane_b32 v250, s43, 24
	v_writelane_b32 v250, s44, 25
	v_writelane_b32 v250, s45, 26
	v_writelane_b32 v250, s46, 27
	v_writelane_b32 v250, s47, 28
	v_writelane_b32 v250, s48, 29
	v_writelane_b32 v250, s49, 30
	v_writelane_b32 v250, s50, 31
	v_writelane_b32 v250, s51, 32
	v_writelane_b32 v250, s52, 33
	v_writelane_b32 v250, s53, 34
	v_writelane_b32 v250, s54, 35
	v_writelane_b32 v250, s56, 36
	v_writelane_b32 v250, s57, 37
	v_writelane_b32 v250, vcc_lo, 38
	v_writelane_b32 v250, vcc_hi, 39
	v_mov_b32_e32 v2, v0
	s_mul_i32 s4, s71, 7
	s_movk_i32 s2, 0x6000
	v_readfirstlane_b32 s5, v2
	s_movk_i32 s3, 0x2000
	s_ashr_i32 s5, s5, 6
	s_add_i32 s5, s5, s4
	s_add_i32 s5, s5, 0x31ff
	s_cmpk_gt_i32 s5, 0x38ff
	s_cbranch_scc1 .Lb2_end
	s_add_u32 s9, s26, 0x4800000
	s_addc_u32 s18, s27, 0
	s_add_u32 s19, s26, 0x2800000
	v_and_b32_e32 v1, 56, v2
	v_lshlrev_b32_e32 v2, 2, v2
	s_addc_u32 s20, s27, 0
	v_and_b32_e32 v10, 28, v2
	s_lshl_b32 s21, s5, 6
	s_lshl_b32 s22, s2, 6
	s_lshl_b32 s23, s5, 5
	s_lshl_b32 s40, s2, 5
	s_lshl_b32 s41, s5, 3
	s_lshl_b32 s42, s2, 3
	s_lshl_b32 s43, s5, 1
	s_lshl_b32 s44, s2, 1
	s_add_i32 s45, 0, 0x202a8
	s_waitcnt lgkmcnt(1)
	v_mov_b32_e32 v7, 0
	s_movk_i32 s46, 0x1000
	s_movk_i32 s47, 0x4000
	s_movk_i32 s48, 0x6000
	s_movk_i32 s49, 0x7000
	s_mov_b32 s4, 0x41800000
	s_movk_i32 s50, 0x7fff
	s_mov_b32 s51, 0xffff0000
	s_mov_b64 s[10:11], 0x600
	s_add_i32 s52, 0, 0x202a0
	s_add_i32 s53, 0, 0x20298
	v_mov_b32_e32 v11, 1
	v_mov_b32_e32 v12, 0x400
	v_mov_b32_e32 v13, 0x7c
	s_branch .Lb2_07

; #define LAS __attribute__((address_space(3)))
; template <class T> __device__ __forceinline__ T* wsp(const Frame& F, size_t off) { return (T*)(F.ws + off); }
; __device__ __forceinline__ void xcd_barrier(const XcdBarrier& b) {
;     asm volatile("s_waitcnt vmcnt(0)" ::: "memory");
;     __syncthreads();
;     if (threadIdx.x == 0) {
;         unsigned* bar = b.bar;
;         __builtin_amdgcn_s_waitcnt(0);
;     LAS float* scr = (LAS float*)(F.lds + RING_OFF + F.wave * 16384);
;     const int gw = (ncu ? (int)blockIdx.x - cu0 : F.vcu) * NWAVES + F.wave, NGW = (ncu ? ncu : F.G) * NWAVES;
;     bf16* UP = wsp<bf16>(F, WS_WEUP); bf16* DN = wsp<bf16>(F, WS_WEDN);
;     for (int it = it0 + gw; it < it1; it += NGW) {
;         const int e = it / 384, r = it % 384; const size_t eo = (size_t)(layer * 64 + e) * 1024 * 256;
;         if (r < 128) p0_transpose_item(inp(F, I_WGATE) + eo, 1024, 256, UP + (size_t)e * 512 * 1024, 3, scr, r, F.lane);
;         else if (r < 256) p0_transpose_item(inp(F, I_WUP) + eo, 1024, 256, UP + (size_t)e * 512 * 1024, 4, scr, r - 128, F.lane);
;         else p0_transpose_item(inp(F, I_WDOWN) + eo, 256, 1024, DN + (size_t)e * 1024 * 256, 5, scr, r - 256, F.lane, 16.f);
.Lb3_entry:
	s_mov_b64 exec, s[0:1]
	s_cmpk_lg_i32 s67, 0x100
	s_cbranch_scc1 .Lb3_out
	v_writelane_b32 v250, s2, 0
	v_writelane_b32 v250, s3, 1
	v_writelane_b32 v250, s4, 2
	v_writelane_b32 v250, s5, 3
	v_writelane_b32 v250, s9, 4
	v_writelane_b32 v250, s10, 5
	v_writelane_b32 v250, s11, 6
	v_writelane_b32 v250, s12, 7
	v_writelane_b32 v250, s13, 8
	v_writelane_b32 v250, s14, 9
	v_writelane_b32 v250, s15, 10
	v_writelane_b32 v250, s16, 11
	v_writelane_b32 v250, s17, 12
	v_writelane_b32 v250, s18, 13
	v_writelane_b32 v250, s19, 14
	v_writelane_b32 v250, s20, 15
	v_writelane_b32 v250, s21, 16
	v_writelane_b32 v250, s22, 17
	v_writelane_b32 v250, s23, 18
	v_writelane_b32 v250, s30, 19
	v_writelane_b32 v250, s31, 20
	v_writelane_b32 v250, s40, 21
	v_writelane_b32 v250, s41, 22
	v_writelane_b32 v250, s42, 23
	v_writelane_b32 v250, s43, 24
	v_writelane_b32 v250, s44, 25
	v_writelane_b32 v250, s45, 26
	v_writelane_b32 v250, s46, 27
	v_writelane_b32 v250, s47, 28
	v_writelane_b32 v250, s48, 29
	v_writelane_b32 v250, s49, 30
	v_writelane_b32 v250, s50, 31
	v_writelane_b32 v250, s51, 32
	v_writelane_b32 v250, s52, 33
	v_writelane_b32 v250, s53, 34
	v_writelane_b32 v250, s54, 35
	v_writelane_b32 v250, s56, 36
	v_writelane_b32 v250, s57, 37
	v_writelane_b32 v250, vcc_lo, 38
	v_writelane_b32 v250, vcc_hi, 39
	v_mov_b32_e32 v2, v0
	s_mul_i32 s4, s71, 7
	s_movk_i32 s2, 0x6000
	v_readfirstlane_b32 s5, v2
	s_movk_i32 s3, 0x2000
	s_ashr_i32 s5, s5, 6
	s_add_i32 s5, s5, s4
	s_add_i32 s5, s5, 0x38ff
	s_cmpk_gt_i32 s5, 0x3fff
	s_cbranch_scc1 .Lb3_end
	s_add_u32 s9, s26, 0x4800000
	s_addc_u32 s18, s27, 0
	s_add_u32 s19, s26, 0x2800000
	v_and_b32_e32 v1, 56, v2
	v_lshlrev_b32_e32 v2, 2, v2
	s_addc_u32 s20, s27, 0
	v_and_b32_e32 v10, 28, v2
	s_lshl_b32 s21, s5, 6
	s_lshl_b32 s22, s2, 6
	s_lshl_b32 s23, s5, 5
	s_lshl_b32 s40, s2, 5
	s_lshl_b32 s41, s5, 3
	s_lshl_b32 s42, s2, 3
	s_lshl_b32 s43, s5, 1
	s_lshl_b32 s44, s2, 1
	s_add_i32 s45, 0, 0x202a8
	s_waitcnt lgkmcnt(1)
	v_mov_b32_e32 v7, 0
	s_movk_i32 s46, 0x1000
	s_movk_i32 s47, 0x4000
	s_movk_i32 s48, 0x6000
	s_movk_i32 s49, 0x7000
	s_mov_b32 s4, 0x41800000
	s_movk_i32 s50, 0x7fff
	s_mov_b32 s51, 0xffff0000
	s_mov_b64 s[10:11], 0x600
	s_add_i32 s52, 0, 0x202a0
	s_add_i32 s53, 0, 0x20298
	v_mov_b32_e32 v11, 1
	v_mov_b32_e32 v12, 0x400
	v_mov_b32_e32 v13, 0x7c
	s_branch .Lb3_07

; #define LAS __attribute__((address_space(3)))
; template <class T> __device__ __forceinline__ T* wsp(const Frame& F, size_t off) { return (T*)(F.ws + off); }
; __device__ __forceinline__ void xcd_barrier(const XcdBarrier& b) {
;     asm volatile("s_waitcnt vmcnt(0)" ::: "memory");
;     __syncthreads();
;     if (threadIdx.x == 0) {
;         unsigned* bar = b.bar;
;         __builtin_amdgcn_s_waitcnt(0);
;     LAS float* scr = (LAS float*)(F.lds + RING_OFF + F.wave * 16384);
;     const int gw = (ncu ? (int)blockIdx.x - cu0 : F.vcu) * NWAVES + F.wave, NGW = (ncu ? ncu : F.G) * NWAVES;
;     bf16* UP = wsp<bf16>(F, WS_WEUP); bf16* DN = wsp<bf16>(F, WS_WEDN);
;     for (int it = it0 + gw; it < it1; it += NGW) {
;         const int e = it / 384, r = it % 384; const size_t eo = (size_t)(layer * 64 + e) * 1024 * 256;
;         if (r < 128) p0_transpose_item(inp(F, I_WGATE) + eo, 1024, 256, UP + (size_t)e * 512 * 1024, 3, scr, r, F.lane);
;         else if (r < 256) p0_transpose_item(inp(F, I_WUP) + eo, 1024, 256, UP + (size_t)e * 512 * 1024, 4, scr, r - 128, F.lane);
;         else p0_transpose_item(inp(F, I_WDOWN) + eo, 256, 1024, DN + (size_t)e * 1024 * 256, 5, scr, r - 256, F.lane, 16.f);
.Lb4_entry:
	s_mov_b64 exec, s[0:1]
	s_cmpk_lg_i32 s67, 0x100
	s_cbranch_scc1 .Lb4_out
	v_writelane_b32 v250, s2, 0
	v_writelane_b32 v250, s3, 1
	v_writelane_b32 v250, s4, 2
	v_writelane_b32 v250, s5, 3
	v_writelane_b32 v250, s9, 4
	v_writelane_b32 v250, s10, 5
	v_writelane_b32 v250, s11, 6
	v_writelane_b32 v250, s12, 7
	v_writelane_b32 v250, s13, 8
	v_writelane_b32 v250, s14, 9
	v_writelane_b32 v250, s15, 10
	v_writelane_b32 v250, s16, 11
	v_writelane_b32 v250, s17, 12
	v_writelane_b32 v250, s18, 13
	v_writelane_b32 v250, s19, 14
	v_writelane_b32 v250, s20, 15
	v_writelane_b32 v250, s21, 16
	v_writelane_b32 v250, s22, 17
	v_writelane_b32 v250, s23, 18
	v_writelane_b32 v250, s30, 19
	v_writelane_b32 v250, s31, 20
	v_writelane_b32 v250, s40, 21
	v_writelane_b32 v250, s41, 22
	v_writelane_b32 v250, s42, 23
	v_writelane_b32 v250, s43, 24
	v_writelane_b32 v250, s44, 25
	v_writelane_b32 v250, s45, 26
	v_writelane_b32 v250, s46, 27
	v_writelane_b32 v250, s47, 28
	v_writelane_b32 v250, s48, 29
	v_writelane_b32 v250, s49, 30
	v_writelane_b32 v250, s50, 31
	v_writelane_b32 v250, s51, 32
	v_writelane_b32 v250, s52, 33
	v_writelane_b32 v250, s53, 34
	v_writelane_b32 v250, s54, 35
	v_writelane_b32 v250, s56, 36
	v_writelane_b32 v250, s57, 37
	v_writelane_b32 v250, vcc_lo, 38
	v_writelane_b32 v250, vcc_hi, 39
	v_mov_b32_e32 v2, v0
	s_mul_i32 s4, s71, 7
	s_movk_i32 s2, 0x6000
	v_readfirstlane_b32 s5, v2
	s_movk_i32 s3, 0x2000
	s_ashr_i32 s5, s5, 6
	s_add_i32 s5, s5, s4
	s_add_i32 s5, s5, 0x3fff
	s_cmpk_gt_i32 s5, 0x46ff
	s_cbranch_scc1 .Lb4_end
	s_add_u32 s9, s26, 0x4800000
	s_addc_u32 s18, s27, 0
	s_add_u32 s19, s26, 0x2800000
	v_and_b32_e32 v1, 56, v2
	v_lshlrev_b32_e32 v2, 2, v2
	s_addc_u32 s20, s27, 0
	v_and_b32_e32 v10, 28, v2
	s_lshl_b32 s21, s5, 6
	s_lshl_b32 s22, s2, 6
	s_lshl_b32 s23, s5, 5
	s_lshl_b32 s40, s2, 5
	s_lshl_b32 s41, s5, 3
	s_lshl_b32 s42, s2, 3
	s_lshl_b32 s43, s5, 1
	s_lshl_b32 s44, s2, 1
	s_add_i32 s45, 0, 0x202a8
	s_waitcnt lgkmcnt(1)
	v_mov_b32_e32 v7, 0
	s_movk_i32 s46, 0x1000
	s_movk_i32 s47, 0x4000
	s_movk_i32 s48, 0x6000
	s_movk_i32 s49, 0x7000
	s_mov_b32 s4, 0x41800000
	s_movk_i32 s50, 0x7fff
	s_mov_b32 s51, 0xffff0000
	s_mov_b64 s[10:11], 0x600
	s_add_i32 s52, 0, 0x202a0
	s_add_i32 s53, 0, 0x20298
	v_mov_b32_e32 v11, 1
	v_mov_b32_e32 v12, 0x400
	v_mov_b32_e32 v13, 0x7c
	s_branch .Lb4_07

; #define LAS __attribute__((address_space(3)))
; template <class T> __device__ __forceinline__ T* wsp(const Frame& F, size_t off) { return (T*)(F.ws + off); }
; __device__ __forceinline__ void xcd_barrier(const XcdBarrier& b) {
;     asm volatile("s_waitcnt vmcnt(0)" ::: "memory");
;     __syncthreads();
;     if (threadIdx.x == 0) {
;         unsigned* bar = b.bar;
;         __builtin_amdgcn_s_waitcnt(0);
;     LAS float* scr = (LAS float*)(F.lds + RING_OFF + F.wave * 16384);
;     const int gw = (ncu ? (int)blockIdx.x - cu0 : F.vcu) * NWAVES + F.wave, NGW = (ncu ? ncu : F.G) * NWAVES;
;     bf16* UP = wsp<bf16>(F, WS_WEUP); bf16* DN = wsp<bf16>(F, WS_WEDN);
;     for (int it = it0 + gw; it < it1; it += NGW) {
;         const int e = it / 384, r = it % 384; const size_t eo = (size_t)(layer * 64 + e) * 1024 * 256;
;         if (r < 128) p0_transpose_item(inp(F, I_WGATE) + eo, 1024, 256, UP + (size_t)e * 512 * 1024, 3, scr, r, F.lane);
;         else if (r < 256) p0_transpose_item(inp(F, I_WUP) + eo, 1024, 256, UP + (size_t)e * 512 * 1024, 4, scr, r - 128, F.lane);
;         else p0_transpose_item(inp(F, I_WDOWN) + eo, 256, 1024, DN + (size_t)e * 1024 * 256, 5, scr, r - 256, F.lane, 16.f);
.Lb5_entry:
	s_mov_b64 exec, s[0:1]
	s_cmpk_lg_i32 s67, 0x100
	s_cbranch_scc1 .Lb5_out
	v_writelane_b32 v250, s2, 0
	v_writelane_b32 v250, s3, 1
	v_writelane_b32 v250, s4, 2
	v_writelane_b32 v250, s5, 3
	v_writelane_b32 v250, s9, 4
	v_writelane_b32 v250, s10, 5
	v_writelane_b32 v250, s11, 6
	v_writelane_b32 v250, s12, 7
	v_writelane_b32 v250, s13, 8
	v_writelane_b32 v250, s14, 9
	v_writelane_b32 v250, s15, 10
	v_writelane_b32 v250, s16, 11
	v_writelane_b32 v250, s17, 12
	v_writelane_b32 v250, s18, 13
	v_writelane_b32 v250, s19, 14
	v_writelane_b32 v250, s20, 15
	v_writelane_b32 v250, s21, 16
	v_writelane_b32 v250, s22, 17
	v_writelane_b32 v250, s23, 18
	v_writelane_b32 v250, s30, 19
	v_writelane_b32 v250, s31, 20
	v_writelane_b32 v250, s40, 21
	v_writelane_b32 v250, s41, 22
	v_writelane_b32 v250, s42, 23
	v_writelane_b32 v250, s43, 24
	v_writelane_b32 v250, s44, 25
	v_writelane_b32 v250, s45, 26
	v_writelane_b32 v250, s46, 27
	v_writelane_b32 v250, s47, 28
	v_writelane_b32 v250, s48, 29
	v_writelane_b32 v250, s49, 30
	v_writelane_b32 v250, s50, 31
	v_writelane_b32 v250, s51, 32
	v_writelane_b32 v250, s52, 33
	v_writelane_b32 v250, s53, 34
	v_writelane_b32 v250, s54, 35
	v_writelane_b32 v250, s56, 36
	v_writelane_b32 v250, s57, 37
	v_writelane_b32 v250, vcc_lo, 38
	v_writelane_b32 v250, vcc_hi, 39
	v_mov_b32_e32 v2, v0
	s_mul_i32 s4, s71, 7
	s_movk_i32 s2, 0x6000
	v_readfirstlane_b32 s5, v2
	s_movk_i32 s3, 0x2000
	s_ashr_i32 s5, s5, 6
	s_add_i32 s5, s5, s4
	s_add_i32 s5, s5, 0x46ff
	s_cmpk_gt_i32 s5, 0x4dff
	s_cbranch_scc1 .Lb5_end
	s_add_u32 s9, s26, 0x4800000
	s_addc_u32 s18, s27, 0
	s_add_u32 s19, s26, 0x2800000
	v_and_b32_e32 v1, 56, v2
	v_lshlrev_b32_e32 v2, 2, v2
	s_addc_u32 s20, s27, 0
	v_and_b32_e32 v10, 28, v2
	s_lshl_b32 s21, s5, 6
	s_lshl_b32 s22, s2, 6
	s_lshl_b32 s23, s5, 5
	s_lshl_b32 s40, s2, 5
	s_lshl_b32 s41, s5, 3
	s_lshl_b32 s42, s2, 3
	s_lshl_b32 s43, s5, 1
	s_lshl_b32 s44, s2, 1
	s_add_i32 s45, 0, 0x202a8
	s_waitcnt lgkmcnt(1)
	v_mov_b32_e32 v7, 0
	s_movk_i32 s46, 0x1000
	s_movk_i32 s47, 0x4000
	s_movk_i32 s48, 0x6000
	s_movk_i32 s49, 0x7000
	s_mov_b32 s4, 0x41800000
	s_movk_i32 s50, 0x7fff
	s_mov_b32 s51, 0xffff0000
	s_mov_b64 s[10:11], 0x600
	s_add_i32 s52, 0, 0x202a0
	s_add_i32 s53, 0, 0x20298
	v_mov_b32_e32 v11, 1
	v_mov_b32_e32 v12, 0x400
	v_mov_b32_e32 v13, 0x7c
	s_branch .Lb5_07

; #define LAS __attribute__((address_space(3)))
; template <class T> __device__ __forceinline__ T* wsp(const Frame& F, size_t off) { return (T*)(F.ws + off); }
;     LAS float* scr = (LAS float*)(F.lds + RING_OFF + F.wave * 16384);
;     const int gw = (ncu ? (int)blockIdx.x - cu0 : F.vcu) * NWAVES + F.wave, NGW = (ncu ? ncu : F.G) * NWAVES;
;     bf16* UP = wsp<bf16>(F, WS_WEUP); bf16* DN = wsp<bf16>(F, WS_WEDN);
;     for (int it = it0 + gw; it < it1; it += NGW) {
;         const int e = it / 384, r = it % 384; const size_t eo = (size_t)(layer * 64 + e) * 1024 * 256;
;         if (r < 128) p0_transpose_item(inp(F, I_WGATE) + eo, 1024, 256, UP + (size_t)e * 512 * 1024, 3, scr, r, F.lane);
;         else if (r < 256) p0_transpose_item(inp(F, I_WUP) + eo, 1024, 256, UP + (size_t)e * 512 * 1024, 4, scr, r - 128, F.lane);
;         else p0_transpose_item(inp(F, I_WDOWN) + eo, 256, 1024, DN + (size_t)e * 1024 * 256, 5, scr, r - 256, F.lane, 16.f);
.Lcv0_entry:
	s_cmpk_lg_i32 s67, 0x100
	s_cbranch_scc1 .Lcv0_end
	v_mov_b32_e32 v2, v0
	s_mul_i32 s4, s71, 5
	s_movk_i32 s2, 0x500
	v_readfirstlane_b32 s5, v2
	s_movk_i32 s3, 0x2000
	s_ashr_i32 s5, s5, 6
	s_cmpk_lt_i32 s5, 3
	s_cbranch_scc1 .Lcv0_end
	s_add_i32 s5, s5, s4
	s_addk_i32 s5, 0x4dfd
	s_cmpk_gt_i32 s5, 0x5fff
	s_cbranch_scc1 .Lcv0_end
	s_add_u32 s9, s38, 0x4800000
	s_addc_u32 s18, s39, 0
	s_add_u32 s19, s38, 0x2800000
	v_and_b32_e32 v1, 56, v2
	v_lshlrev_b32_e32 v2, 2, v2
	s_addc_u32 s20, s39, 0
	v_and_b32_e32 v10, 28, v2
	s_lshl_b32 s21, s5, 6
	s_lshl_b32 s22, s2, 6
	s_lshl_b32 s23, s5, 5
	s_lshl_b32 s40, s2, 5
	s_lshl_b32 s41, s5, 3
	s_lshl_b32 s42, s2, 3
	s_lshl_b32 s43, s5, 1
	s_lshl_b32 s44, s2, 1
	s_add_i32 s45, 0, 0x202a8
	s_waitcnt lgkmcnt(1)
	v_mov_b32_e32 v7, 0
	s_movk_i32 s46, 0x1000
	s_movk_i32 s47, 0x4000
	s_movk_i32 s48, 0x6000
	s_movk_i32 s49, 0x7000
	s_mov_b32 s4, 0x41800000
	s_movk_i32 s50, 0x7fff
	s_mov_b32 s51, 0xffff0000
	s_mov_b64 s[10:11], 0x600
	s_add_i32 s52, 0, 0x202a0
	s_add_i32 s53, 0, 0x20298
	v_mov_b32_e32 v11, 1
	v_mov_b32_e32 v12, 0x400
	v_mov_b32_e32 v13, 0x7c
	s_branch .Lcv0_07

; #define LAS __attribute__((address_space(3)))
; template <class T> __device__ __forceinline__ T* wsp(const Frame& F, size_t off) { return (T*)(F.ws + off); }
; __device__ __forceinline__ void xcd_barrier(const XcdBarrier& b) {
;     asm volatile("s_waitcnt vmcnt(0)" ::: "memory");
;     __syncthreads();
;     if (threadIdx.x == 0) {
;         unsigned* bar = b.bar;
;         __builtin_amdgcn_s_waitcnt(0);
;     LAS float* scr = (LAS float*)(F.lds + RING_OFF + F.wave * 16384);
;     const int gw = (ncu ? (int)blockIdx.x - cu0 : F.vcu) * NWAVES + F.wave, NGW = (ncu ? ncu : F.G) * NWAVES;
;     bf16* UP = wsp<bf16>(F, WS_WEUP); bf16* DN = wsp<bf16>(F, WS_WEDN);
;     for (int it = it0 + gw; it < it1; it += NGW) {
;         const int e = it / 384, r = it % 384; const size_t eo = (size_t)(layer * 64 + e) * 1024 * 256;
;         if (r < 128) p0_transpose_item(inp(F, I_WGATE) + eo, 1024, 256, UP + (size_t)e * 512 * 1024, 3, scr, r, F.lane);
;         else if (r < 256) p0_transpose_item(inp(F, I_WUP) + eo, 1024, 256, UP + (size_t)e * 512 * 1024, 4, scr, r - 128, F.lane);
;         else p0_transpose_item(inp(F, I_WDOWN) + eo, 256, 1024, DN + (size_t)e * 1024 * 256, 5, scr, r - 256, F.lane, 16.f);
.Lb9_entry:
	s_mov_b64 exec, s[0:1]
	s_cmpk_lg_i32 s67, 0x100
	s_cbranch_scc1 .Lb9_out
	v_writelane_b32 v250, s2, 0
	v_writelane_b32 v250, s3, 1
	v_writelane_b32 v250, s4, 2
	v_writelane_b32 v250, s5, 3
	v_writelane_b32 v250, s9, 4
	v_writelane_b32 v250, s10, 5
	v_writelane_b32 v250, s11, 6
	v_writelane_b32 v250, s12, 7
	v_writelane_b32 v250, s13, 8
	v_writelane_b32 v250, s14, 9
	v_writelane_b32 v250, s15, 10
	v_writelane_b32 v250, s16, 11
	v_writelane_b32 v250, s17, 12
	v_writelane_b32 v250, s18, 13
	v_writelane_b32 v250, s19, 14
	v_writelane_b32 v250, s20, 15
	v_writelane_b32 v250, s21, 16
	v_writelane_b32 v250, s22, 17
	v_writelane_b32 v250, s23, 18
	v_writelane_b32 v250, s30, 19
	v_writelane_b32 v250, s31, 20
	v_writelane_b32 v250, s40, 21
	v_writelane_b32 v250, s41, 22
	v_writelane_b32 v250, s42, 23
	v_writelane_b32 v250, s43, 24
	v_writelane_b32 v250, s44, 25
	v_writelane_b32 v250, s45, 26
	v_writelane_b32 v250, s46, 27
	v_writelane_b32 v250, s47, 28
	v_writelane_b32 v250, s48, 29
	v_writelane_b32 v250, s49, 30
	v_writelane_b32 v250, s50, 31
	v_writelane_b32 v250, s51, 32
	v_writelane_b32 v250, s52, 33
	v_writelane_b32 v250, s53, 34
	v_writelane_b32 v250, s54, 35
	v_writelane_b32 v250, s56, 36
	v_writelane_b32 v250, s57, 37
	v_writelane_b32 v250, vcc_lo, 38
	v_writelane_b32 v250, vcc_hi, 39
	v_mov_b32_e32 v2, v0
	s_mul_i32 s4, s71, 7
	s_movk_i32 s2, 0x6000
	v_readfirstlane_b32 s5, v2
	s_movk_i32 s3, 0x2000
	s_ashr_i32 s5, s5, 6
	s_add_i32 s5, s5, s4
	s_add_i32 s5, s5, 0x1fff
	s_cmpk_gt_i32 s5, 0x26ff
	s_cbranch_scc1 .Lb9_end
	s_add_u32 s9, s26, 0x4800000
	s_addc_u32 s18, s27, 0
	s_add_u32 s19, s26, 0x2800000
	v_and_b32_e32 v1, 56, v2
	v_lshlrev_b32_e32 v2, 2, v2
	s_addc_u32 s20, s27, 0
	v_and_b32_e32 v10, 28, v2
	s_lshl_b32 s21, s5, 6
	s_lshl_b32 s22, s2, 6
	s_lshl_b32 s23, s5, 5
	s_lshl_b32 s40, s2, 5
	s_lshl_b32 s41, s5, 3
	s_lshl_b32 s42, s2, 3
	s_lshl_b32 s43, s5, 1
	s_lshl_b32 s44, s2, 1
	s_add_i32 s45, 0, 0x202a8
	s_waitcnt lgkmcnt(1)
	v_mov_b32_e32 v7, 0
	s_movk_i32 s46, 0x1000
	s_movk_i32 s47, 0x4000
	s_movk_i32 s48, 0x6000
	s_movk_i32 s49, 0x7000
	s_mov_b32 s4, 0x41800000
	s_movk_i32 s50, 0x7fff
	s_mov_b32 s51, 0xffff0000
	s_mov_b64 s[10:11], 0x600
	s_add_i32 s52, 0, 0x202a0
	s_add_i32 s53, 0, 0x20298
	v_mov_b32_e32 v11, 1
	v_mov_b32_e32 v12, 0x400
	v_mov_b32_e32 v13, 0x7c
	s_branch .Lb9_07

; #define LAS __attribute__((address_space(3)))
; template <class T> __device__ __forceinline__ T* wsp(const Frame& F, size_t off) { return (T*)(F.ws + off); }
; __device__ __forceinline__ void xcd_barrier(const XcdBarrier& b) {
;     asm volatile("s_waitcnt vmcnt(0)" ::: "memory");
;     __syncthreads();
;     if (threadIdx.x == 0) {
;         unsigned* bar = b.bar;
;         __builtin_amdgcn_s_waitcnt(0);
;     LAS float* scr = (LAS float*)(F.lds + RING_OFF + F.wave * 16384);
;     const int gw = (ncu ? (int)blockIdx.x - cu0 : F.vcu) * NWAVES + F.wave, NGW = (ncu ? ncu : F.G) * NWAVES;
;     bf16* UP = wsp<bf16>(F, WS_WEUP); bf16* DN = wsp<bf16>(F, WS_WEDN);
;     for (int it = it0 + gw; it < it1; it += NGW) {
;         const int e = it / 384, r = it % 384; const size_t eo = (size_t)(layer * 64 + e) * 1024 * 256;
;         if (r < 128) p0_transpose_item(inp(F, I_WGATE) + eo, 1024, 256, UP + (size_t)e * 512 * 1024, 3, scr, r, F.lane);
;         else if (r < 256) p0_transpose_item(inp(F, I_WUP) + eo, 1024, 256, UP + (size_t)e * 512 * 1024, 4, scr, r - 128, F.lane);
;         else p0_transpose_item(inp(F, I_WDOWN) + eo, 256, 1024, DN + (size_t)e * 1024 * 256, 5, scr, r - 256, F.lane, 16.f);
.Lb10_entry:
	s_mov_b64 exec, s[2:3]
	s_cmpk_lg_i32 s67, 0x100
	s_cbranch_scc1 .Lb10_out
	v_writelane_b32 v250, s2, 0
	v_writelane_b32 v250, s3, 1
	v_writelane_b32 v250, s4, 2
	v_writelane_b32 v250, s5, 3
	v_writelane_b32 v250, s9, 4
	v_writelane_b32 v250, s10, 5
	v_writelane_b32 v250, s11, 6
	v_writelane_b32 v250, s12, 7
	v_writelane_b32 v250, s13, 8
	v_writelane_b32 v250, s14, 9
	v_writelane_b32 v250, s15, 10
	v_writelane_b32 v250, s16, 11
	v_writelane_b32 v250, s17, 12
	v_writelane_b32 v250, s18, 13
	v_writelane_b32 v250, s19, 14
	v_writelane_b32 v250, s20, 15
	v_writelane_b32 v250, s21, 16
	v_writelane_b32 v250, s22, 17
	v_writelane_b32 v250, s23, 18
	v_writelane_b32 v250, s30, 19
	v_writelane_b32 v250, s31, 20
	v_writelane_b32 v250, s40, 21
	v_writelane_b32 v250, s41, 22
	v_writelane_b32 v250, s42, 23
	v_writelane_b32 v250, s43, 24
	v_writelane_b32 v250, s44, 25
	v_writelane_b32 v250, s45, 26
	v_writelane_b32 v250, s46, 27
	v_writelane_b32 v250, s47, 28
	v_writelane_b32 v250, s48, 29
	v_writelane_b32 v250, s49, 30
	v_writelane_b32 v250, s50, 31
	v_writelane_b32 v250, s51, 32
	v_writelane_b32 v250, s52, 33
	v_writelane_b32 v250, s53, 34
	v_writelane_b32 v250, s54, 35
	v_writelane_b32 v250, s56, 36
	v_writelane_b32 v250, s57, 37
	v_writelane_b32 v250, vcc_lo, 38
	v_writelane_b32 v250, vcc_hi, 39
	v_mov_b32_e32 v2, v0
	s_mul_i32 s4, s71, 7
	s_movk_i32 s2, 0x6000
	v_readfirstlane_b32 s5, v2
	s_movk_i32 s3, 0x2000
	s_ashr_i32 s5, s5, 6
	s_add_i32 s5, s5, s4
	s_add_i32 s5, s5, 0x26ff
	s_cmpk_gt_i32 s5, 0x2dff
	s_cbranch_scc1 .Lb10_end
	s_add_u32 s9, s26, 0x4800000
	s_addc_u32 s18, s27, 0
	s_add_u32 s19, s26, 0x2800000
	v_and_b32_e32 v1, 56, v2
	v_lshlrev_b32_e32 v2, 2, v2
	s_addc_u32 s20, s27, 0
	v_and_b32_e32 v10, 28, v2
	s_lshl_b32 s21, s5, 6
	s_lshl_b32 s22, s2, 6
	s_lshl_b32 s23, s5, 5
	s_lshl_b32 s40, s2, 5
	s_lshl_b32 s41, s5, 3
	s_lshl_b32 s42, s2, 3
	s_lshl_b32 s43, s5, 1
	s_lshl_b32 s44, s2, 1
	s_add_i32 s45, 0, 0x202a8
	s_waitcnt lgkmcnt(1)
	v_mov_b32_e32 v7, 0
	s_movk_i32 s46, 0x1000
	s_movk_i32 s47, 0x4000
	s_movk_i32 s48, 0x6000
	s_movk_i32 s49, 0x7000
	s_mov_b32 s4, 0x41800000
	s_movk_i32 s50, 0x7fff
	s_mov_b32 s51, 0xffff0000
	s_mov_b64 s[10:11], 0x600
	s_add_i32 s52, 0, 0x202a0
	s_add_i32 s53, 0, 0x20298
	v_mov_b32_e32 v11, 1
	v_mov_b32_e32 v12, 0x400
	v_mov_b32_e32 v13, 0x7c
	s_branch .Lb10_07

; #define LAS __attribute__((address_space(3)))
; template <class T> __device__ __forceinline__ T* wsp(const Frame& F, size_t off) { return (T*)(F.ws + off); }
; __device__ __forceinline__ void xcd_barrier(const XcdBarrier& b) {
;     asm volatile("s_waitcnt vmcnt(0)" ::: "memory");
;     __syncthreads();
;     if (threadIdx.x == 0) {
;         unsigned* bar = b.bar;
;         __builtin_amdgcn_s_waitcnt(0);
;     LAS float* scr = (LAS float*)(F.lds + RING_OFF + F.wave * 16384);
;     const int gw = (ncu ? (int)blockIdx.x - cu0 : F.vcu) * NWAVES + F.wave, NGW = (ncu ? ncu : F.G) * NWAVES;
;     bf16* UP = wsp<bf16>(F, WS_WEUP); bf16* DN = wsp<bf16>(F, WS_WEDN);
;     for (int it = it0 + gw; it < it1; it += NGW) {
;         const int e = it / 384, r = it % 384; const size_t eo = (size_t)(layer * 64 + e) * 1024 * 256;
;         if (r < 128) p0_transpose_item(inp(F, I_WGATE) + eo, 1024, 256, UP + (size_t)e * 512 * 1024, 3, scr, r, F.lane);
;         else if (r < 256) p0_transpose_item(inp(F, I_WUP) + eo, 1024, 256, UP + (size_t)e * 512 * 1024, 4, scr, r - 128, F.lane);
;         else p0_transpose_item(inp(F, I_WDOWN) + eo, 256, 1024, DN + (size_t)e * 1024 * 256, 5, scr, r - 256, F.lane, 16.f);
.Lb11_entry:
	s_mov_b64 exec, s[0:1]
	s_cmpk_lg_i32 s67, 0x100
	s_cbranch_scc1 .Lb11_out
	v_writelane_b32 v250, s2, 0
	v_writelane_b32 v250, s3, 1
	v_writelane_b32 v250, s4, 2
	v_writelane_b32 v250, s5, 3
	v_writelane_b32 v250, s9, 4
	v_writelane_b32 v250, s10, 5
	v_writelane_b32 v250, s11, 6
	v_writelane_b32 v250, s12, 7
	v_writelane_b32 v250, s13, 8
	v_writelane_b32 v250, s14, 9
	v_writelane_b32 v250, s15, 10
	v_writelane_b32 v250, s16, 11
	v_writelane_b32 v250, s17, 12
	v_writelane_b32 v250, s18, 13
	v_writelane_b32 v250, s19, 14
	v_writelane_b32 v250, s20, 15
	v_writelane_b32 v250, s21, 16
	v_writelane_b32 v250, s22, 17
	v_writelane_b32 v250, s23, 18
	v_writelane_b32 v250, s30, 19
	v_writelane_b32 v250, s31, 20
	v_writelane_b32 v250, s40, 21
	v_writelane_b32 v250, s41, 22
	v_writelane_b32 v250, s42, 23
	v_writelane_b32 v250, s43, 24
	v_writelane_b32 v250, s44, 25
	v_writelane_b32 v250, s45, 26
	v_writelane_b32 v250, s46, 27
	v_writelane_b32 v250, s47, 28
	v_writelane_b32 v250, s48, 29
	v_writelane_b32 v250, s49, 30
	v_writelane_b32 v250, s50, 31
	v_writelane_b32 v250, s51, 32
	v_writelane_b32 v250, s52, 33
	v_writelane_b32 v250, s53, 34
	v_writelane_b32 v250, s54, 35
	v_writelane_b32 v250, s56, 36
	v_writelane_b32 v250, s57, 37
	v_writelane_b32 v250, vcc_lo, 38
	v_writelane_b32 v250, vcc_hi, 39
	v_mov_b32_e32 v2, v0
	s_mul_i32 s4, s71, 7
	s_movk_i32 s2, 0x6000
	v_readfirstlane_b32 s5, v2
	s_movk_i32 s3, 0x2000
	s_ashr_i32 s5, s5, 6
	s_add_i32 s5, s5, s4
	s_add_i32 s5, s5, 0x2dff
	s_cmpk_gt_i32 s5, 0x34ff
	s_cbranch_scc1 .Lb11_end
	s_add_u32 s9, s26, 0x4800000
	s_addc_u32 s18, s27, 0
	s_add_u32 s19, s26, 0x2800000
	v_and_b32_e32 v1, 56, v2
	v_lshlrev_b32_e32 v2, 2, v2
	s_addc_u32 s20, s27, 0
	v_and_b32_e32 v10, 28, v2
	s_lshl_b32 s21, s5, 6
	s_lshl_b32 s22, s2, 6
	s_lshl_b32 s23, s5, 5
	s_lshl_b32 s40, s2, 5
	s_lshl_b32 s41, s5, 3
	s_lshl_b32 s42, s2, 3
	s_lshl_b32 s43, s5, 1
	s_lshl_b32 s44, s2, 1
	s_add_i32 s45, 0, 0x202a8
	s_waitcnt lgkmcnt(1)
	v_mov_b32_e32 v7, 0
	s_movk_i32 s46, 0x1000
	s_movk_i32 s47, 0x4000
	s_movk_i32 s48, 0x6000
	s_movk_i32 s49, 0x7000
	s_mov_b32 s4, 0x41800000
	s_movk_i32 s50, 0x7fff
	s_mov_b32 s51, 0xffff0000
	s_mov_b64 s[10:11], 0x600
	s_add_i32 s52, 0, 0x202a0
	s_add_i32 s53, 0, 0x20298
	v_mov_b32_e32 v11, 1
	v_mov_b32_e32 v12, 0x400
	v_mov_b32_e32 v13, 0x7c
	s_branch .Lb11_07

; #define LAS __attribute__((address_space(3)))
; template <class T> __device__ __forceinline__ T* wsp(const Frame& F, size_t off) { return (T*)(F.ws + off); }
; __device__ __forceinline__ void xcd_barrier(const XcdBarrier& b) {
;     asm volatile("s_waitcnt vmcnt(0)" ::: "memory");
;     __syncthreads();
;     if (threadIdx.x == 0) {
;         unsigned* bar = b.bar;
;         __builtin_amdgcn_s_waitcnt(0);
;     LAS float* scr = (LAS float*)(F.lds + RING_OFF + F.wave * 16384);
;     const int gw = (ncu ? (int)blockIdx.x - cu0 : F.vcu) * NWAVES + F.wave, NGW = (ncu ? ncu : F.G) * NWAVES;
;     bf16* UP = wsp<bf16>(F, WS_WEUP); bf16* DN = wsp<bf16>(F, WS_WEDN);
;     for (int it = it0 + gw; it < it1; it += NGW) {
;         const int e = it / 384, r = it % 384; const size_t eo = (size_t)(layer * 64 + e) * 1024 * 256;
;         if (r < 128) p0_transpose_item(inp(F, I_WGATE) + eo, 1024, 256, UP + (size_t)e * 512 * 1024, 3, scr, r, F.lane);
;         else if (r < 256) p0_transpose_item(inp(F, I_WUP) + eo, 1024, 256, UP + (size_t)e * 512 * 1024, 4, scr, r - 128, F.lane);
;         else p0_transpose_item(inp(F, I_WDOWN) + eo, 256, 1024, DN + (size_t)e * 1024 * 256, 5, scr, r - 256, F.lane, 16.f);
.Lb12_entry:
	s_mov_b64 exec, s[0:1]
	s_cmpk_lg_i32 s67, 0x100
	s_cbranch_scc1 .Lb12_out
	v_writelane_b32 v250, s2, 0
	v_writelane_b32 v250, s3, 1
	v_writelane_b32 v250, s4, 2
	v_writelane_b32 v250, s5, 3
	v_writelane_b32 v250, s9, 4
	v_writelane_b32 v250, s10, 5
	v_writelane_b32 v250, s11, 6
	v_writelane_b32 v250, s12, 7
	v_writelane_b32 v250, s13, 8
	v_writelane_b32 v250, s14, 9
	v_writelane_b32 v250, s15, 10
	v_writelane_b32 v250, s16, 11
	v_writelane_b32 v250, s17, 12
	v_writelane_b32 v250, s18, 13
	v_writelane_b32 v250, s19, 14
	v_writelane_b32 v250, s20, 15
	v_writelane_b32 v250, s21, 16
	v_writelane_b32 v250, s22, 17
	v_writelane_b32 v250, s23, 18
	v_writelane_b32 v250, s30, 19
	v_writelane_b32 v250, s31, 20
	v_writelane_b32 v250, s40, 21
	v_writelane_b32 v250, s41, 22
	v_writelane_b32 v250, s42, 23
	v_writelane_b32 v250, s43, 24
	v_writelane_b32 v250, s44, 25
	v_writelane_b32 v250, s45, 26
	v_writelane_b32 v250, s46, 27
	v_writelane_b32 v250, s47, 28
	v_writelane_b32 v250, s48, 29
	v_writelane_b32 v250, s49, 30
	v_writelane_b32 v250, s50, 31
	v_writelane_b32 v250, s51, 32
	v_writelane_b32 v250, s52, 33
	v_writelane_b32 v250, s53, 34
	v_writelane_b32 v250, s54, 35
	v_writelane_b32 v250, s56, 36
	v_writelane_b32 v250, s57, 37
	v_writelane_b32 v250, vcc_lo, 38
	v_writelane_b32 v250, vcc_hi, 39
	v_mov_b32_e32 v2, v0
	s_mul_i32 s4, s71, 7
	s_movk_i32 s2, 0x6000
	v_readfirstlane_b32 s5, v2
	s_movk_i32 s3, 0x2000
	s_ashr_i32 s5, s5, 6
	s_add_i32 s5, s5, s4
	s_add_i32 s5, s5, 0x34ff
	s_cmpk_gt_i32 s5, 0x3bff
	s_cbranch_scc1 .Lb12_end
	s_add_u32 s9, s26, 0x4800000
	s_addc_u32 s18, s27, 0
	s_add_u32 s19, s26, 0x2800000
	v_and_b32_e32 v1, 56, v2
	v_lshlrev_b32_e32 v2, 2, v2
	s_addc_u32 s20, s27, 0
	v_and_b32_e32 v10, 28, v2
	s_lshl_b32 s21, s5, 6
	s_lshl_b32 s22, s2, 6
	s_lshl_b32 s23, s5, 5
	s_lshl_b32 s40, s2, 5
	s_lshl_b32 s41, s5, 3
	s_lshl_b32 s42, s2, 3
	s_lshl_b32 s43, s5, 1
	s_lshl_b32 s44, s2, 1
	s_add_i32 s45, 0, 0x202a8
	s_waitcnt lgkmcnt(1)
	v_mov_b32_e32 v7, 0
	s_movk_i32 s46, 0x1000
	s_movk_i32 s47, 0x4000
	s_movk_i32 s48, 0x6000
	s_movk_i32 s49, 0x7000
	s_mov_b32 s4, 0x41800000
	s_movk_i32 s50, 0x7fff
	s_mov_b32 s51, 0xffff0000
	s_mov_b64 s[10:11], 0x600
	s_add_i32 s52, 0, 0x202a0
	s_add_i32 s53, 0, 0x20298
	v_mov_b32_e32 v11, 1
	v_mov_b32_e32 v12, 0x400
	v_mov_b32_e32 v13, 0x7c
	s_branch .Lb12_07

; #define LAS __attribute__((address_space(3)))
; template <class T> __device__ __forceinline__ T* wsp(const Frame& F, size_t off) { return (T*)(F.ws + off); }
; __device__ __forceinline__ void xcd_barrier(const XcdBarrier& b) {
;     asm volatile("s_waitcnt vmcnt(0)" ::: "memory");
;     __syncthreads();
;     if (threadIdx.x == 0) {
;         unsigned* bar = b.bar;
;         __builtin_amdgcn_s_waitcnt(0);
;     LAS float* scr = (LAS float*)(F.lds + RING_OFF + F.wave * 16384);
;     const int gw = (ncu ? (int)blockIdx.x - cu0 : F.vcu) * NWAVES + F.wave, NGW = (ncu ? ncu : F.G) * NWAVES;
;     bf16* UP = wsp<bf16>(F, WS_WEUP); bf16* DN = wsp<bf16>(F, WS_WEDN);
;     for (int it = it0 + gw; it < it1; it += NGW) {
;         const int e = it / 384, r = it % 384; const size_t eo = (size_t)(layer * 64 + e) * 1024 * 256;
;         if (r < 128) p0_transpose_item(inp(F, I_WGATE) + eo, 1024, 256, UP + (size_t)e * 512 * 1024, 3, scr, r, F.lane);
;         else if (r < 256) p0_transpose_item(inp(F, I_WUP) + eo, 1024, 256, UP + (size_t)e * 512 * 1024, 4, scr, r - 128, F.lane);
;         else p0_transpose_item(inp(F, I_WDOWN) + eo, 256, 1024, DN + (size_t)e * 1024 * 256, 5, scr, r - 256, F.lane, 16.f);
.LBB0_1442:
	s_or_b64 exec, exec, s[10:11]
	s_waitcnt vmcnt(0)
	s_branch .LBB0_1443
.Lb13_entry:
	s_mov_b64 exec, s[0:1]
	s_cmpk_lg_i32 s67, 0x100
	s_cbranch_scc1 .Lb13_out
	v_writelane_b32 v250, s2, 0
	v_writelane_b32 v250, s3, 1
	v_writelane_b32 v250, s4, 2
	v_writelane_b32 v250, s5, 3
	v_writelane_b32 v250, s9, 4
	v_writelane_b32 v250, s10, 5
	v_writelane_b32 v250, s11, 6
	v_writelane_b32 v250, s12, 7
	v_writelane_b32 v250, s13, 8
	v_writelane_b32 v250, s14, 9
	v_writelane_b32 v250, s15, 10
	v_writelane_b32 v250, s16, 11
	v_writelane_b32 v250, s17, 12
	v_writelane_b32 v250, s18, 13
	v_writelane_b32 v250, s19, 14
	v_writelane_b32 v250, s20, 15
	v_writelane_b32 v250, s21, 16
	v_writelane_b32 v250, s22, 17
	v_writelane_b32 v250, s23, 18
	v_writelane_b32 v250, s30, 19
	v_writelane_b32 v250, s31, 20
	v_writelane_b32 v250, s40, 21
	v_writelane_b32 v250, s41, 22
	v_writelane_b32 v250, s42, 23
	v_writelane_b32 v250, s43, 24
	v_writelane_b32 v250, s44, 25
	v_writelane_b32 v250, s45, 26
	v_writelane_b32 v250, s46, 27
	v_writelane_b32 v250, s47, 28
	v_writelane_b32 v250, s48, 29
	v_writelane_b32 v250, s49, 30
	v_writelane_b32 v250, s50, 31
	v_writelane_b32 v250, s51, 32
	v_writelane_b32 v250, s52, 33
	v_writelane_b32 v250, s53, 34
	v_writelane_b32 v250, s54, 35
	v_writelane_b32 v250, s56, 36
	v_writelane_b32 v250, s57, 37
	v_writelane_b32 v250, vcc_lo, 38
	v_writelane_b32 v250, vcc_hi, 39
	v_mov_b32_e32 v2, v0
	s_mul_i32 s4, s71, 7
	s_movk_i32 s2, 0x6000
	v_readfirstlane_b32 s5, v2
	s_movk_i32 s3, 0x2000
	s_ashr_i32 s5, s5, 6
	s_add_i32 s5, s5, s4
	s_add_i32 s5, s5, 0x3bff
	s_cmpk_gt_i32 s5, 0x42ff
	s_cbranch_scc1 .Lb13_end
	s_add_u32 s9, s26, 0x4800000
	s_addc_u32 s18, s27, 0
	s_add_u32 s19, s26, 0x2800000
	v_and_b32_e32 v1, 56, v2
	v_lshlrev_b32_e32 v2, 2, v2
	s_addc_u32 s20, s27, 0
	v_and_b32_e32 v10, 28, v2
	s_lshl_b32 s21, s5, 6
	s_lshl_b32 s22, s2, 6
	s_lshl_b32 s23, s5, 5
	s_lshl_b32 s40, s2, 5
	s_lshl_b32 s41, s5, 3
	s_lshl_b32 s42, s2, 3
	s_lshl_b32 s43, s5, 1
	s_lshl_b32 s44, s2, 1
	s_add_i32 s45, 0, 0x202a8
	s_waitcnt lgkmcnt(1)
	v_mov_b32_e32 v7, 0
	s_movk_i32 s46, 0x1000
	s_movk_i32 s47, 0x4000
	s_movk_i32 s48, 0x6000
	s_movk_i32 s49, 0x7000
	s_mov_b32 s4, 0x41800000
	s_movk_i32 s50, 0x7fff
	s_mov_b32 s51, 0xffff0000
	s_mov_b64 s[10:11], 0x600
	s_add_i32 s52, 0, 0x202a0
	s_add_i32 s53, 0, 0x20298
	v_mov_b32_e32 v11, 1
	v_mov_b32_e32 v12, 0x400
	v_mov_b32_e32 v13, 0x7c
	s_branch .Lb13_07

; #define LAS __attribute__((address_space(3)))
; template <class T> __device__ __forceinline__ T* wsp(const Frame& F, size_t off) { return (T*)(F.ws + off); }
; __device__ __forceinline__ void xcd_barrier(const XcdBarrier& b) {
;     asm volatile("s_waitcnt vmcnt(0)" ::: "memory");
;     __syncthreads();
;     if (threadIdx.x == 0) {
;         unsigned* bar = b.bar;
;         __builtin_amdgcn_s_waitcnt(0);
;     LAS float* scr = (LAS float*)(F.lds + RING_OFF + F.wave * 16384);
;     const int gw = (ncu ? (int)blockIdx.x - cu0 : F.vcu) * NWAVES + F.wave, NGW = (ncu ? ncu : F.G) * NWAVES;
;     bf16* UP = wsp<bf16>(F, WS_WEUP); bf16* DN = wsp<bf16>(F, WS_WEDN);
;     for (int it = it0 + gw; it < it1; it += NGW) {
;         const int e = it / 384, r = it % 384; const size_t eo = (size_t)(layer * 64 + e) * 1024 * 256;
;         if (r < 128) p0_transpose_item(inp(F, I_WGATE) + eo, 1024, 256, UP + (size_t)e * 512 * 1024, 3, scr, r, F.lane);
;         else if (r < 256) p0_transpose_item(inp(F, I_WUP) + eo, 1024, 256, UP + (size_t)e * 512 * 1024, 4, scr, r - 128, F.lane);
;         else p0_transpose_item(inp(F, I_WDOWN) + eo, 256, 1024, DN + (size_t)e * 1024 * 256, 5, scr, r - 256, F.lane, 16.f);
.Lb14_entry:
	s_mov_b64 exec, s[0:1]
	s_cmpk_lg_i32 s67, 0x100
	s_cbranch_scc1 .Lb14_out
	v_writelane_b32 v250, s2, 0
	v_writelane_b32 v250, s3, 1
	v_writelane_b32 v250, s4, 2
	v_writelane_b32 v250, s5, 3
	v_writelane_b32 v250, s9, 4
	v_writelane_b32 v250, s10, 5
	v_writelane_b32 v250, s11, 6
	v_writelane_b32 v250, s12, 7
	v_writelane_b32 v250, s13, 8
	v_writelane_b32 v250, s14, 9
	v_writelane_b32 v250, s15, 10
	v_writelane_b32 v250, s16, 11
	v_writelane_b32 v250, s17, 12
	v_writelane_b32 v250, s18, 13
	v_writelane_b32 v250, s19, 14
	v_writelane_b32 v250, s20, 15
	v_writelane_b32 v250, s21, 16
	v_writelane_b32 v250, s22, 17
	v_writelane_b32 v250, s23, 18
	v_writelane_b32 v250, s30, 19
	v_writelane_b32 v250, s31, 20
	v_writelane_b32 v250, s40, 21
	v_writelane_b32 v250, s41, 22
	v_writelane_b32 v250, s42, 23
	v_writelane_b32 v250, s43, 24
	v_writelane_b32 v250, s44, 25
	v_writelane_b32 v250, s45, 26
	v_writelane_b32 v250, s46, 27
	v_writelane_b32 v250, s47, 28
	v_writelane_b32 v250, s48, 29
	v_writelane_b32 v250, s49, 30
	v_writelane_b32 v250, s50, 31
	v_writelane_b32 v250, s51, 32
	v_writelane_b32 v250, s52, 33
	v_writelane_b32 v250, s53, 34
	v_writelane_b32 v250, s54, 35
	v_writelane_b32 v250, s56, 36
	v_writelane_b32 v250, s57, 37
	v_writelane_b32 v250, vcc_lo, 38
	v_writelane_b32 v250, vcc_hi, 39
	v_mov_b32_e32 v2, v0
	s_mul_i32 s4, s71, 7
	s_movk_i32 s2, 0x6000
	v_readfirstlane_b32 s5, v2
	s_movk_i32 s3, 0x2000
	s_ashr_i32 s5, s5, 6
	s_add_i32 s5, s5, s4
	s_add_i32 s5, s5, 0x42ff
	s_cmpk_gt_i32 s5, 0x49ff
	s_cbranch_scc1 .Lb14_end
	s_add_u32 s9, s26, 0x4800000
	s_addc_u32 s18, s27, 0
	s_add_u32 s19, s26, 0x2800000
	v_and_b32_e32 v1, 56, v2
	v_lshlrev_b32_e32 v2, 2, v2
	s_addc_u32 s20, s27, 0
	v_and_b32_e32 v10, 28, v2
	s_lshl_b32 s21, s5, 6
	s_lshl_b32 s22, s2, 6
	s_lshl_b32 s23, s5, 5
	s_lshl_b32 s40, s2, 5
	s_lshl_b32 s41, s5, 3
	s_lshl_b32 s42, s2, 3
	s_lshl_b32 s43, s5, 1
	s_lshl_b32 s44, s2, 1
	s_add_i32 s45, 0, 0x202a8
	s_waitcnt lgkmcnt(1)
	v_mov_b32_e32 v7, 0
	s_movk_i32 s46, 0x1000
	s_movk_i32 s47, 0x4000
	s_movk_i32 s48, 0x6000
	s_movk_i32 s49, 0x7000
	s_mov_b32 s4, 0x41800000
	s_movk_i32 s50, 0x7fff
	s_mov_b32 s51, 0xffff0000
	s_mov_b64 s[10:11], 0x600
	s_add_i32 s52, 0, 0x202a0
	s_add_i32 s53, 0, 0x20298
	v_mov_b32_e32 v11, 1
	v_mov_b32_e32 v12, 0x400
	v_mov_b32_e32 v13, 0x7c
	s_branch .Lb14_07

; #define LAS __attribute__((address_space(3)))
; template <class T> __device__ __forceinline__ T* wsp(const Frame& F, size_t off) { return (T*)(F.ws + off); }
;     LAS float* scr = (LAS float*)(F.lds + RING_OFF + F.wave * 16384);
;     const int gw = (ncu ? (int)blockIdx.x - cu0 : F.vcu) * NWAVES + F.wave, NGW = (ncu ? ncu : F.G) * NWAVES;
;     bf16* UP = wsp<bf16>(F, WS_WEUP); bf16* DN = wsp<bf16>(F, WS_WEDN);
;     for (int it = it0 + gw; it < it1; it += NGW) {
;         const int e = it / 384, r = it % 384; const size_t eo = (size_t)(layer * 64 + e) * 1024 * 256;
;         if (r < 128) p0_transpose_item(inp(F, I_WGATE) + eo, 1024, 256, UP + (size_t)e * 512 * 1024, 3, scr, r, F.lane);
;         else if (r < 256) p0_transpose_item(inp(F, I_WUP) + eo, 1024, 256, UP + (size_t)e * 512 * 1024, 4, scr, r - 128, F.lane);
;         else p0_transpose_item(inp(F, I_WDOWN) + eo, 256, 1024, DN + (size_t)e * 1024 * 256, 5, scr, r - 256, F.lane, 16.f);
.Lcv1_entry:
	s_cmpk_lg_i32 s67, 0x100
	s_cbranch_scc1 .Lcv1_end
	v_mov_b32_e32 v2, v0
	s_mul_i32 s4, s71, 6
	s_movk_i32 s2, 0x600
	v_readfirstlane_b32 s5, v2
	s_movk_i32 s3, 0x2000
	s_ashr_i32 s5, s5, 6
	s_add_i32 s5, s5, s4
	s_addk_i32 s5, 0x49fe
	s_cmpk_gt_i32 s5, 0x5fff
	s_cbranch_scc1 .Lcv1_end
	s_add_u32 s9, s38, 0x4800000
	s_addc_u32 s18, s39, 0
	s_add_u32 s19, s38, 0x2800000
	v_and_b32_e32 v1, 56, v2
	v_lshlrev_b32_e32 v2, 2, v2
	s_addc_u32 s20, s39, 0
	v_and_b32_e32 v10, 28, v2
	s_lshl_b32 s21, s5, 6
	s_lshl_b32 s22, s2, 6
	s_lshl_b32 s23, s5, 5
	s_lshl_b32 s40, s2, 5
	s_lshl_b32 s41, s5, 3
	s_lshl_b32 s42, s2, 3
	s_lshl_b32 s43, s5, 1
	s_lshl_b32 s44, s2, 1
	s_add_i32 s45, 0, 0x202a8
	s_waitcnt lgkmcnt(1)
	v_mov_b32_e32 v7, 0
	s_movk_i32 s46, 0x1000
	s_movk_i32 s47, 0x4000
	s_movk_i32 s48, 0x6000
	s_movk_i32 s49, 0x7000
	s_mov_b32 s4, 0x41800000
	s_movk_i32 s50, 0x7fff
	s_mov_b32 s51, 0xffff0000
	s_mov_b64 s[10:11], 0x600
	s_add_i32 s52, 0, 0x202a0
	s_add_i32 s53, 0, 0x20298
	v_mov_b32_e32 v11, 1
	v_mov_b32_e32 v12, 0x400
	v_mov_b32_e32 v13, 0x7c
	s_branch .Lcv1_07
